# gla_s_chain start-of-segment state scan: the 24 loads of a step requested together with counted vmcnt waits (was one vmcnt(0) round trip per load pair); on top of m11
# speedup vs baseline: 1.0213x; 1.0023x over previous
; #define GAS __attribute__((address_space(1)))
; DI void gla_s_chain(LAS unsigned char* lds, const Ctx& c, int l, int bl, int h, int seg) {
;     ...
;     for (int j = 0; j < seg; ++j) {
;         const int cj = (bl * 4 + h) * NSEG + j;
;         const GAS f32x4* sl = (const GAS f32x4*)(c.ws + WS_SLOC) + ((size_t)(cj * 8 + w) * 16) * 64 + lane; const GAS f32x4* dq = (const GAS f32x4*)(c.ws + WS_DCUM) + (size_t)cj * 8 * 64 + lane;
; #pragma unroll
;         for (int a = 0; a < 8; ++a) { const f32x4 dcv = dq[a * 64]; S[a][0] = S[a][0] * dcv + sl[(a * 2) * 64]; S[a][1] = S[a][1] * dcv + sl[(a * 2 + 1) * 64]; }
;     }
.LBB0_751:
	s_ashr_i32 s41, s40, 31
	s_lshl_b64 s[6:7], s[40:41], 14
	v_lshl_add_u64 v[76:77], v[58:59], 0, s[42:43]
	v_lshl_add_u64 v[60:61], v[2:3], 0, s[6:7]
	v_add_co_u32_e32 v84, vcc, 0x1000, v76
	s_nop 1
	v_addc_co_u32_e32 v85, vcc, 0, v77, vcc
	v_add_co_u32_e32 v78, vcc, 0x1000, v60
	s_nop 1
	v_addc_co_u32_e32 v79, vcc, 0, v61, vcc
	v_add_co_u32_e32 v80, vcc, 0x2000, v60
	s_nop 1
	v_addc_co_u32_e32 v81, vcc, 0, v61, vcc
	v_add_co_u32_e32 v82, vcc, 0x3000, v60
	s_nop 1
	v_addc_co_u32_e32 v83, vcc, 0, v61, vcc
	global_load_dwordx4 v[86:89], v[76:77], off
	global_load_dwordx4 v[66:69], v[60:61], off
	global_load_dwordx4 v[70:73], v[60:61], off offset:1024
	global_load_dwordx4 v[90:93], v[76:77], off offset:1024
	global_load_dwordx4 v[136:139], v[60:61], off offset:2048
	global_load_dwordx4 v[140:143], v[60:61], off offset:3072
	global_load_dwordx4 v[94:97], v[76:77], off offset:2048
	global_load_dwordx4 v[146:149], v[78:79], off
	global_load_dwordx4 v[150:153], v[78:79], off offset:1024
	global_load_dwordx4 v[98:101], v[76:77], off offset:3072
	global_load_dwordx4 v[154:157], v[78:79], off offset:2048
	global_load_dwordx4 v[158:161], v[78:79], off offset:3072
	global_load_dwordx4 v[102:105], v[84:85], off
	global_load_dwordx4 v[162:165], v[80:81], off
	global_load_dwordx4 v[166:169], v[80:81], off offset:1024
	global_load_dwordx4 v[106:109], v[84:85], off offset:1024
	global_load_dwordx4 v[170:173], v[80:81], off offset:2048
	global_load_dwordx4 v[174:177], v[80:81], off offset:3072
	global_load_dwordx4 v[110:113], v[84:85], off offset:2048
	global_load_dwordx4 v[178:181], v[82:83], off
	global_load_dwordx4 v[182:185], v[82:83], off offset:1024
	global_load_dwordx4 v[114:117], v[84:85], off offset:3072
	global_load_dwordx4 v[186:189], v[82:83], off offset:2048
	s_add_u32 s42, s42, 0x2000
	s_addc_u32 s43, s43, 0
	s_add_i32 s40, s40, 8
	s_waitcnt vmcnt(21)
	v_pk_fma_f32 v[20:21], v[20:21], v[88:89], v[68:69]
	v_pk_fma_f32 v[18:19], v[18:19], v[86:87], v[66:67]
	global_load_dwordx4 v[66:69], v[82:83], off offset:3072
	s_waitcnt vmcnt(21)
	v_pk_fma_f32 v[16:17], v[16:17], v[88:89], v[72:73]
	v_pk_fma_f32 v[14:15], v[14:15], v[86:87], v[70:71]
	s_waitcnt vmcnt(19)
	v_pk_fma_f32 v[28:29], v[28:29], v[92:93], v[138:139]
	v_pk_fma_f32 v[26:27], v[26:27], v[90:91], v[136:137]
	s_waitcnt vmcnt(18)
	v_pk_fma_f32 v[24:25], v[24:25], v[92:93], v[142:143]
	v_pk_fma_f32 v[22:23], v[22:23], v[90:91], v[140:141]
	s_waitcnt vmcnt(16)
	v_pk_fma_f32 v[36:37], v[36:37], v[96:97], v[148:149]
	v_pk_fma_f32 v[34:35], v[34:35], v[94:95], v[146:147]
	s_waitcnt vmcnt(15)
	v_pk_fma_f32 v[32:33], v[32:33], v[96:97], v[152:153]
	v_pk_fma_f32 v[30:31], v[30:31], v[94:95], v[150:151]
	s_waitcnt vmcnt(13)
	v_pk_fma_f32 v[44:45], v[44:45], v[100:101], v[156:157]
	v_pk_fma_f32 v[42:43], v[42:43], v[98:99], v[154:155]
	s_waitcnt vmcnt(12)
	v_pk_fma_f32 v[40:41], v[40:41], v[100:101], v[160:161]
	v_pk_fma_f32 v[38:39], v[38:39], v[98:99], v[158:159]
	s_waitcnt vmcnt(10)
	v_pk_fma_f32 v[52:53], v[52:53], v[104:105], v[164:165]
	v_pk_fma_f32 v[50:51], v[50:51], v[102:103], v[162:163]
	s_waitcnt vmcnt(9)
	v_pk_fma_f32 v[48:49], v[48:49], v[104:105], v[168:169]
	v_pk_fma_f32 v[46:47], v[46:47], v[102:103], v[166:167]
	s_waitcnt vmcnt(7)
	v_pk_fma_f32 v[134:135], v[134:135], v[108:109], v[172:173]
	v_pk_fma_f32 v[132:133], v[132:133], v[106:107], v[170:171]
	s_waitcnt vmcnt(6)
	v_pk_fma_f32 v[130:131], v[130:131], v[108:109], v[176:177]
	v_pk_fma_f32 v[128:129], v[128:129], v[106:107], v[174:175]
	s_waitcnt vmcnt(4)
	v_pk_fma_f32 v[64:65], v[64:65], v[112:113], v[180:181]
	v_pk_fma_f32 v[62:63], v[62:63], v[110:111], v[178:179]
	s_waitcnt vmcnt(3)
	v_pk_fma_f32 v[56:57], v[56:57], v[112:113], v[184:185]
	v_pk_fma_f32 v[54:55], v[54:55], v[110:111], v[182:183]
	s_waitcnt vmcnt(1)
	v_pk_fma_f32 v[126:127], v[126:127], v[116:117], v[188:189]
	v_pk_fma_f32 v[124:125], v[124:125], v[114:115], v[186:187]
	s_waitcnt vmcnt(0)
	v_pk_fma_f32 v[120:121], v[120:121], v[116:117], v[68:69]
	v_pk_fma_f32 v[122:123], v[122:123], v[114:115], v[66:67]
	s_cmp_eq_u32 s4, s42
	s_cbranch_scc0 .LBB0_751
	s_branch .LBB0_753
